# baseline (speedup 1.0000x reference)
_Z16sum_layer_kernelPKfS0_Pf:
	s_load_dwordx4 s[4:7], s[0:1], 0x0
	s_load_dwordx2 s[8:9], s[0:1], 0x10
	v_lshrrev_b32_e32 v42, 6, v0
	v_bfe_u32 v41, v0, 5, 1
	v_and_b32_e32 v40, 31, v0
	v_readfirstlane_b32 s23, v42
	v_and_b32_e32 v43, 7, v0
	v_bfe_u32 v44, v0, 3, 3
	s_lshl_b32 s3, s2, 12
	s_lshl_b32 s19, s2, 7
	s_lshl_b32 s23, s23, 12
	v_lshlrev_b32_e32 v1, 11, v41
	v_lshl_or_b32 v1, v40, 2, v1
	s_mov_b32 m0, s23
	v_lshrrev_b32_e32 v46, 1, v44
	v_xor_b32_e32 v46, v43, v46
	v_lshlrev_b32_e32 v46, 4, v46
	v_lshl_add_u32 v35, v44, 16, v46
	v_lshl_add_u32 v35, v42, 21, v35
	v_add_u32_e32 v35, s19, v35
	v_xor_b32_e32 v86, 64, v35
	s_mov_b32 s20, 0x7fc00
	s_mov_b32 s21, 0xff800
	s_mov_b32 s22, 0x17f400
	s_mov_b32 s14, 0x200000
	s_mov_b32 s15, 0x20000
	v_and_b32_e32 v45, 63, v0
	v_lshlrev_b32_e32 v37, 4, v45
	s_add_u32 s54, s23, 0x4000
	s_waitcnt lgkmcnt(0)
	s_mov_b32 s12, s6
	s_and_b32 s13, s7, 0xffff
	s_and_b32 s5, s5, 0xffff
	s_mov_b32 s6, 0x800000
	s_mov_b32 s7, s15
	buffer_load_dwordx4 v35, s[4:7], 0 offen nt lds
	buffer_load_dwordx4 v86, s[4:7], s20 offen offset:1024 nt lds
	buffer_load_dwordx4 v35, s[4:7], s21 offen offset:2048 nt lds
	buffer_load_dwordx4 v86, s[4:7], s22 offen offset:3072 nt lds
	s_mov_b32 m0, s54
	s_nop 0
	buffer_load_dwordx4 v37, s[12:15], s3 offen nt lds
	buffer_load_dwordx4 v37, s[12:15], s3 offen offset:1024 nt lds
	buffer_load_dwordx4 v37, s[12:15], s3 offen offset:2048 nt lds
	buffer_load_dwordx4 v37, s[12:15], s3 offen offset:3072 nt lds
	v_and_b32_e32 v45, 63, v0
	v_lshlrev_b32_e32 v36, 2, v40
	v_lshl_add_u32 v36, v41, 18, v36
	v_lshl_add_u32 v36, v42, 21, v36
	v_add_u32_e32 v36, s19, v36
	v_bfe_u32 v47, v40, 1, 3
	v_lshlrev_b32_e32 v39, 2, v41
	v_xor_b32_e32 v39, v39, v47
	v_lshlrev_b32_e32 v39, 4, v39
	v_lshl_add_u32 v39, v40, 7, v39
	v_lshl_add_u32 v39, v42, 12, v39
	v_xor_b32_e32 v81, 16, v39
	v_xor_b32_e32 v82, 32, v39
	v_xor_b32_e32 v83, 48, v39
	v_cmp_gt_u32_e32 vcc, 32, v45
	v_mov_b32_e32 v34, 0xc1600000
	v_mov_b32_e32 v84, 0x3fb8aa3b
	v_mov_b32_e32 v85, 0x3f317218
	s_lshl_b32 s24, 1, 16
	s_lshl_b32 s25, 2, 16
	s_lshl_b32 s26, 3, 16
	s_lshl_b32 s27, 8, 16
	s_lshl_b32 s28, 9, 16
	s_lshl_b32 s29, 10, 16
	s_lshl_b32 s30, 11, 16
	s_lshl_b32 s31, 16, 16
	s_lshl_b32 s32, 17, 16
	s_lshl_b32 s33, 18, 16
	s_lshl_b32 s34, 19, 16
	s_lshl_b32 s35, 24, 16
	s_lshl_b32 s36, 25, 16
	s_lshl_b32 s37, 26, 16
	s_lshl_b32 s38, 27, 16
	s_and_b32 s9, s9, 0xffff
	s_mov_b32 s10, s6
	s_mov_b32 s11, s15
	v_lshl_add_u32 v38, v42, 12, v1
	v_add_u32_e32 v38, 0x4000, v38
	v_add_u32_e32 v87, 0x400, v38
	s_waitcnt vmcnt(0)
	ds_read2_b32 v[18:19], v38 offset0:0 offset1:32
	ds_read2_b32 v[20:21], v38 offset0:64 offset1:96
	ds_read2_b32 v[22:23], v38 offset0:128 offset1:160
	ds_read2_b32 v[24:25], v38 offset0:192 offset1:224
	ds_read2_b32 v[26:27], v87 offset0:0 offset1:32
	ds_read2_b32 v[28:29], v87 offset0:64 offset1:96
	ds_read2_b32 v[30:31], v87 offset0:128 offset1:160
	ds_read2_b32 v[32:33], v87 offset0:192 offset1:224
	s_waitcnt lgkmcnt(0)
	v_max3_f32 v48, v18, v19, v20
	v_max3_f32 v50, v21, v22, v23
	v_max3_f32 v48, v48, v24, v25
	v_max3_f32 v50, v50, v26, v27
	v_max3_f32 v48, v48, v28, v29
	v_max3_f32 v50, v50, v30, v31
	v_max3_f32 v48, v48, v32, v33
	v_max_f32_e32 v48, v48, v50
	v_mov_b32_e32 v50, v48
	s_nop 1
	v_permlane32_swap_b32_e32 v48, v50
	v_max_f32_e32 v48, v48, v50
	v_fmamk_f32 v48, v48, 0x3fb8aa3b, v34
	v_pk_fma_f32 v[18:19], v[18:19], v[84:85], v[48:49] op_sel_hi:[1,0,0] neg_lo:[0,0,1] neg_hi:[0,0,1]
	v_exp_f32_e32 v18, v18
	v_exp_f32_e32 v19, v19
	v_pk_fma_f32 v[20:21], v[20:21], v[84:85], v[48:49] op_sel_hi:[1,0,0] neg_lo:[0,0,1] neg_hi:[0,0,1]
	v_exp_f32_e32 v20, v20
	v_exp_f32_e32 v21, v21
	v_pk_fma_f32 v[22:23], v[22:23], v[84:85], v[48:49] op_sel_hi:[1,0,0] neg_lo:[0,0,1] neg_hi:[0,0,1]
	v_exp_f32_e32 v22, v22
	v_exp_f32_e32 v23, v23
	v_pk_fma_f32 v[24:25], v[24:25], v[84:85], v[48:49] op_sel_hi:[1,0,0] neg_lo:[0,0,1] neg_hi:[0,0,1]
	v_exp_f32_e32 v24, v24
	v_exp_f32_e32 v25, v25
	v_pk_fma_f32 v[26:27], v[26:27], v[84:85], v[48:49] op_sel_hi:[1,0,0] neg_lo:[0,0,1] neg_hi:[0,0,1]
	v_exp_f32_e32 v26, v26
	v_exp_f32_e32 v27, v27
	v_pk_fma_f32 v[28:29], v[28:29], v[84:85], v[48:49] op_sel_hi:[1,0,0] neg_lo:[0,0,1] neg_hi:[0,0,1]
	v_exp_f32_e32 v28, v28
	v_exp_f32_e32 v29, v29
	v_pk_fma_f32 v[30:31], v[30:31], v[84:85], v[48:49] op_sel_hi:[1,0,0] neg_lo:[0,0,1] neg_hi:[0,0,1]
	v_exp_f32_e32 v30, v30
	v_exp_f32_e32 v31, v31
	v_pk_fma_f32 v[32:33], v[32:33], v[84:85], v[48:49] op_sel_hi:[1,0,0] neg_lo:[0,0,1] neg_hi:[0,0,1]
	v_exp_f32_e32 v32, v32
	v_exp_f32_e32 v33, v33
	v_pk_add_f32 v[56:57], v[18:19], v[20:21]
	v_pk_add_f32 v[58:59], v[22:23], v[24:25]
	v_pk_add_f32 v[60:61], v[26:27], v[28:29]
	v_pk_add_f32 v[62:63], v[30:31], v[32:33]
	v_pk_add_f32 v[56:57], v[56:57], v[58:59]
	v_pk_add_f32 v[60:61], v[60:61], v[62:63]
	v_pk_add_f32 v[56:57], v[56:57], v[60:61]
	v_add_f32_e32 v50, v56, v57
	v_mov_b32_e32 v51, v50
	s_nop 1
	v_permlane32_swap_b32_e32 v50, v51
	v_add_f32_e32 v50, v50, v51
	v_log_f32_e32 v50, v50
	v_cvt_pk_f16_f32 v40, v18, v19
	v_cvt_pk_f16_f32 v41, v20, v21
	v_cvt_pk_f16_f32 v42, v22, v23
	v_cvt_pk_f16_f32 v43, v24, v25
	v_cvt_pk_f16_f32 v44, v26, v27
	v_cvt_pk_f16_f32 v45, v28, v29
	v_cvt_pk_f16_f32 v46, v30, v31
	v_cvt_pk_f16_f32 v47, v32, v33
	v_add_f32_e32 v50, 0x41600000, v50
	v_mul_f32_e32 v50, 0xbf317218, v50
	v_cndmask_b32_e64 v51, v50, 1.0, vcc
	s_waitcnt vmcnt(0)
	ds_read_b128 v[2:5], v39
	ds_read_b128 v[6:9], v81
	ds_read_b128 v[10:13], v82
	ds_read_b128 v[14:17], v83
	s_waitcnt lgkmcnt(2)
	v_max3_f32 v52, v2, v3, v4
	v_max3_f32 v53, v5, v6, v7
	v_max_f32_e32 v52, v52, v8
	v_max_f32_e32 v53, v53, v9
	s_waitcnt lgkmcnt(0)
	v_max3_f32 v52, v52, v10, v11
	v_max3_f32 v53, v53, v12, v13
	v_max3_f32 v52, v52, v14, v15
	v_max3_f32 v53, v53, v16, v17
	v_max_f32_e32 v52, v52, v53
	v_mov_b32_e32 v53, v52
	s_nop 1
	v_permlane32_swap_b32_e32 v52, v53
	v_max_f32_e32 v52, v52, v53
	v_cndmask_b32_e32 v54, 1.0, v52, vcc
	v_fmamk_f32 v48, v52, 0x3fb8aa3b, v34
	v_pk_fma_f32 v[2:3], v[2:3], v[84:85], v[48:49] op_sel_hi:[1,0,0] neg_lo:[0,0,1] neg_hi:[0,0,1]
	v_mfma_f32_32x32x2_f32 v[64:79], v54, v51, 0
	v_exp_f32_e32 v2, v2
	v_exp_f32_e32 v3, v3
	v_pk_fma_f32 v[4:5], v[4:5], v[84:85], v[48:49] op_sel_hi:[1,0,0] neg_lo:[0,0,1] neg_hi:[0,0,1]
	v_exp_f32_e32 v4, v4
	v_exp_f32_e32 v5, v5
	v_pk_fma_f32 v[6:7], v[6:7], v[84:85], v[48:49] op_sel_hi:[1,0,0] neg_lo:[0,0,1] neg_hi:[0,0,1]
	v_exp_f32_e32 v6, v6
	v_exp_f32_e32 v7, v7
	v_pk_fma_f32 v[8:9], v[8:9], v[84:85], v[48:49] op_sel_hi:[1,0,0] neg_lo:[0,0,1] neg_hi:[0,0,1]
	v_exp_f32_e32 v8, v8
	v_exp_f32_e32 v9, v9
	v_pk_fma_f32 v[10:11], v[10:11], v[84:85], v[48:49] op_sel_hi:[1,0,0] neg_lo:[0,0,1] neg_hi:[0,0,1]
	v_exp_f32_e32 v10, v10
	v_cvt_pk_f16_f32 v56, v2, v3
	v_cvt_pk_f16_f32 v57, v4, v5
	v_cvt_pk_f16_f32 v58, v6, v7
	v_cvt_pk_f16_f32 v59, v8, v9
	v_exp_f32_e32 v11, v11
	v_pk_fma_f32 v[12:13], v[12:13], v[84:85], v[48:49] op_sel_hi:[1,0,0] neg_lo:[0,0,1] neg_hi:[0,0,1]
	v_exp_f32_e32 v12, v12
	v_mfma_f32_32x32x16_f16 v[18:33], v[56:59], v[40:43], 0
	v_exp_f32_e32 v13, v13
	v_pk_fma_f32 v[14:15], v[14:15], v[84:85], v[48:49] op_sel_hi:[1,0,0] neg_lo:[0,0,1] neg_hi:[0,0,1]
	v_exp_f32_e32 v14, v14
	v_exp_f32_e32 v15, v15
	v_pk_fma_f32 v[16:17], v[16:17], v[84:85], v[48:49] op_sel_hi:[1,0,0] neg_lo:[0,0,1] neg_hi:[0,0,1]
	v_exp_f32_e32 v16, v16
	v_exp_f32_e32 v17, v17
	v_cvt_pk_f16_f32 v60, v10, v11
	v_cvt_pk_f16_f32 v61, v12, v13
	v_cvt_pk_f16_f32 v62, v14, v15
	v_cvt_pk_f16_f32 v63, v16, v17
	s_nop 1
	v_mfma_f32_32x32x16_f16 v[18:33], v[60:63], v[44:47], v[18:33]
	s_nop 11
	v_log_f32_e32 v18, v18
	v_log_f32_e32 v19, v19
	v_log_f32_e32 v20, v20
	v_log_f32_e32 v21, v21
	v_log_f32_e32 v22, v22
	v_log_f32_e32 v23, v23
	v_pk_fma_f32 v[64:65], v[18:19], v[84:85], v[64:65] op_sel:[0,1,0] op_sel_hi:[1,1,1]
	buffer_store_dword v64, v36, s[8:11], 0 offen
	buffer_store_dword v65, v36, s[8:11], s24 offen
	v_log_f32_e32 v24, v24
	v_log_f32_e32 v25, v25
	v_pk_fma_f32 v[66:67], v[20:21], v[84:85], v[66:67] op_sel:[0,1,0] op_sel_hi:[1,1,1]
	buffer_store_dword v66, v36, s[8:11], s25 offen
	buffer_store_dword v67, v36, s[8:11], s26 offen
	v_log_f32_e32 v26, v26
	v_log_f32_e32 v27, v27
	v_pk_fma_f32 v[68:69], v[22:23], v[84:85], v[68:69] op_sel:[0,1,0] op_sel_hi:[1,1,1]
	buffer_store_dword v68, v36, s[8:11], s27 offen
	buffer_store_dword v69, v36, s[8:11], s28 offen
	v_log_f32_e32 v28, v28
	v_log_f32_e32 v29, v29
	v_pk_fma_f32 v[70:71], v[24:25], v[84:85], v[70:71] op_sel:[0,1,0] op_sel_hi:[1,1,1]
	buffer_store_dword v70, v36, s[8:11], s29 offen
	buffer_store_dword v71, v36, s[8:11], s30 offen
	v_log_f32_e32 v30, v30
	v_log_f32_e32 v31, v31
	v_pk_fma_f32 v[72:73], v[26:27], v[84:85], v[72:73] op_sel:[0,1,0] op_sel_hi:[1,1,1]
	buffer_store_dword v72, v36, s[8:11], s31 offen
	buffer_store_dword v73, v36, s[8:11], s32 offen
	v_log_f32_e32 v32, v32
	v_log_f32_e32 v33, v33
	v_pk_fma_f32 v[74:75], v[28:29], v[84:85], v[74:75] op_sel:[0,1,0] op_sel_hi:[1,1,1]
	buffer_store_dword v74, v36, s[8:11], s33 offen
	buffer_store_dword v75, v36, s[8:11], s34 offen
	v_pk_fma_f32 v[76:77], v[30:31], v[84:85], v[76:77] op_sel:[0,1,0] op_sel_hi:[1,1,1]
	buffer_store_dword v76, v36, s[8:11], s35 offen
	buffer_store_dword v77, v36, s[8:11], s36 offen
	v_pk_fma_f32 v[78:79], v[32:33], v[84:85], v[78:79] op_sel:[0,1,0] op_sel_hi:[1,1,1]
	buffer_store_dword v78, v36, s[8:11], s37 offen
	buffer_store_dword v79, v36, s[8:11], s38 offen
	s_endpgm
